# GQA attention: q pre-scaled by SCALE*log2e, softmax without running-max shift (bounded scores after qk-rmsnorm), scalar-base staging loads
# speedup vs baseline: 1.0051x; 1.0051x over previous
.LBB0_878:
	s_lshl_b32 s3, s2, 8
	s_add_i32 s33, s3, s29
	s_mul_i32 s8, s69, s33
	s_mul_hi_u32 s9, s68, s33
	s_add_i32 s9, s9, s8
	s_mul_i32 s8, s68, s33
	s_lshl_b64 s[8:9], s[8:9], 1
	s_add_u32 s10, s60, s8
	s_mul_i32 s8, s28, s26
	s_addc_u32 s11, s61, s9
	s_ashr_i32 s9, s8, 31
	s_lshl_b64 s[8:9], s[8:9], 1
	s_add_u32 s8, s10, s8
	s_addc_u32 s9, s11, s9
	s_abs_i32 s11, s28
	s_mul_hi_u32 s12, s11, s25
	s_mul_i32 s13, s12, s89
	s_sub_i32 s11, s11, s13
	s_ashr_i32 s10, s28, 31
	s_add_i32 s13, s12, 1
	s_sub_i32 s14, s11, s89
	s_cmp_ge_u32 s11, s89
	s_cselect_b32 s12, s13, s12
	s_cselect_b32 s11, s14, s11
	s_add_i32 s13, s12, 1
	s_cmp_ge_u32 s11, s89
	s_cselect_b32 s11, s13, s12
	s_xor_b32 s11, s11, s10
	s_waitcnt vmcnt(0)
	s_barrier
	v_mbcnt_lo_u32_b32 v0, -1, 0
	v_mbcnt_hi_u32_b32 v0, -1, v0
	s_sub_i32 s10, s11, s10
	v_add_u32_e32 v184, s80, v0
	s_mul_i32 s10, s10, s27
	s_ashr_i32 s11, s10, 31
	v_ashrrev_i32_e32 v18, 1, v184
	v_bfi_b32 v0, s84, v18, v184
	v_ashrrev_i32_e32 v1, 31, v18
	s_lshl_b64 s[12:13], s[10:11], 1
	v_mul_lo_u32 v3, s69, v0
	v_mul_lo_u32 v4, s68, v1
	v_mad_u64_u32 v[0:1], s[10:11], s68, v0, 0
	v_bfe_u32 v2, v184, 5, 1
	v_add3_u32 v1, v1, v4, v3
	v_lshl_add_u64 v[0:1], v[0:1], 1, s[8:9]
	v_lshlrev_b32_e32 v162, 4, v2
	v_mov_b32_e32 v163, v129
	v_lshl_add_u64 v[16:17], v[0:1], 0, v[162:163]
	s_add_u32 s8, s21, s12
	v_ashrrev_i32_e32 v185, 4, v184
	v_lshlrev_b32_e32 v0, 3, v184
	s_addc_u32 s9, s22, s13
	v_and_b32_e32 v186, 0x78, v0
	v_mul_lo_u32 v0, v185, s62
	s_add_u32 s10, s23, s12
	v_or_b32_e32 v1, v0, v186
	v_add_u32_e32 v0, s38, v0
	s_addc_u32 s11, s24, s13
	v_lshlrev_b32_e32 v128, 1, v1
	v_or_b32_e32 v0, v0, v186
	global_load_dwordx4 v[174:177], v[16:17], off offset:64
	global_load_dwordx4 v[156:159], v[16:17], off offset:96
	global_load_dwordx4 v[188:191], v[16:17], off offset:192
	global_load_dwordx4 v[164:167], v[16:17], off offset:224
	v_lshlrev_b32_e32 v198, 1, v0
	global_load_dwordx4 v[8:11], v128, s[10:11]
	global_load_dwordx4 v[4:7], v128, s[8:9]
	global_load_dwordx4 v[12:15], v198, s[10:11]
	global_load_dwordx4 v[0:3], v198, s[8:9]
	global_load_dwordx4 v[200:203], v[16:17], off
	global_load_dwordx4 v[204:207], v[16:17], off offset:32
	global_load_dwordx4 v[208:211], v[16:17], off offset:128
	global_load_dwordx4 v[212:215], v[16:17], off offset:160
	s_add_i32 s16, s3, 0xffffff00
	s_cmp_eq_u32 s2, 0
	s_cselect_b64 s[14:15], -1, 0
	s_and_b64 s[2:3], s[14:15], exec
	s_cselect_b32 s2, -1, s16
	v_and_b32_e32 v163, 31, v184
	v_and_b32_e32 v18, 0xffffffe0, v18
	s_max_i32 s3, s2, 0
	v_add3_u32 v16, v163, s3, v18
	v_ashrrev_i32_e32 v17, 31, v16
	v_lshlrev_b64 v[16:17], 8, v[16:17]
	v_lshl_add_u64 v[16:17], s[70:71], 0, v[16:17]
	v_and_b32_e32 v84, 32, v184
	v_mov_b32_e32 v85, v129
	v_lshl_add_u64 v[20:21], v[16:17], 0, v[84:85]
	s_mov_b32 s3, 0x80000
	v_add_co_u32_e32 v22, vcc, s3, v20
	s_mov_b64 s[16:17], 0x80040
	v_lshl_add_u64 v[16:17], v[20:21], 0, s[40:41]
	v_addc_co_u32_e32 v23, vcc, 0, v21, vcc
	v_lshl_add_u64 v[28:29], v[20:21], 0, s[16:17]
	s_mov_b64 s[16:17], 0x800c0
	global_load_dwordx4 v[60:63], v[20:21], off offset:16
	global_load_dwordx4 v[72:75], v[20:21], off
	global_load_dwordx4 v[76:79], v[22:23], off
	global_load_dwordx4 v[68:71], v[16:17], off offset:16
	global_load_dwordx4 v[48:51], v[20:21], off offset:80
	global_load_dwordx4 v[56:59], v[20:21], off offset:64
	global_load_dwordx4 v[32:35], v[20:21], off offset:144
	global_load_dwordx4 v[40:43], v[20:21], off offset:128
	v_lshl_add_u64 v[36:37], v[20:21], 0, s[44:45]
	global_load_dwordx4 v[64:67], v[22:23], off offset:64
	global_load_dwordx4 v[44:47], v[22:23], off offset:128
	global_load_dwordx4 v[16:19], v[20:21], off offset:208
	global_load_dwordx4 v[24:27], v[20:21], off offset:192
	v_lshl_add_u64 v[20:21], v[20:21], 0, s[16:17]
	global_load_dwordx4 v[52:55], v[28:29], off offset:16
	s_nop 0
	global_load_dwordx4 v[28:31], v[22:23], off offset:192
	s_nop 0
	global_load_dwordx4 v[36:39], v[36:37], off offset:16
	s_nop 0
	global_load_dwordx4 v[20:23], v[20:21], off offset:16
	global_load_dwordx4 v[142:145], v84, s[58:59]
	global_load_dwordx4 v[138:141], v84, s[58:59] offset:16
	global_load_dwordx4 v[134:137], v84, s[58:59] offset:64
	global_load_dwordx4 v[130:133], v84, s[58:59] offset:80
	global_load_dwordx4 v[124:127], v84, s[58:59] offset:128
	global_load_dwordx4 v[120:123], v84, s[58:59] offset:144
	global_load_dwordx4 v[116:119], v84, s[58:59] offset:192
	global_load_dwordx4 v[112:115], v84, s[58:59] offset:208
	global_load_dwordx4 v[104:107], v84, s[58:59] offset:272
	global_load_dwordx4 v[108:111], v84, s[58:59] offset:256
	global_load_dwordx4 v[96:99], v84, s[58:59] offset:336
	global_load_dwordx4 v[100:103], v84, s[58:59] offset:320
	global_load_dwordx4 v[88:91], v84, s[58:59] offset:400
	global_load_dwordx4 v[92:95], v84, s[58:59] offset:384
	global_load_dwordx4 v[80:83], v84, s[58:59] offset:464
	s_nop 0
	global_load_dwordx4 v[84:87], v84, s[58:59] offset:448
	s_mov_b32 s3, 0x800000
	s_cmp_lt_i32 s2, 0
	s_waitcnt vmcnt(43)
	v_and_b32_e32 v179, 0xffff0000, v177
	v_lshlrev_b32_e32 v178, 16, v177
	v_and_b32_e32 v183, 0xffff0000, v176
	s_waitcnt vmcnt(35)
	v_and_b32_e32 v177, 0xffff0000, v200
	v_lshlrev_b32_e32 v182, 16, v176
	v_lshlrev_b32_e32 v176, 16, v200
	v_mul_f32_e32 v200, v177, v177
	v_and_b32_e32 v171, 0xffff0000, v201
	v_lshlrev_b32_e32 v170, 16, v201
	v_pk_fma_f32 v[200:201], v[176:177], v[176:177], v[200:201] op_sel_hi:[1,1,0]
	v_mul_f32_e32 v224, v171, v171
	v_pk_fma_f32 v[200:201], v[170:171], v[170:171], v[200:201]
	v_and_b32_e32 v151, 0xffff0000, v165
	v_lshlrev_b32_e32 v150, 16, v165
	v_and_b32_e32 v153, 0xffff0000, v164
	v_lshlrev_b32_e32 v152, 16, v164
	v_and_b32_e32 v165, 0xffff0000, v202
	v_lshlrev_b32_e32 v164, 16, v202
	v_pk_add_f32 v[200:201], v[224:225], v[200:201] op_sel_hi:[0,1]
	v_pk_fma_f32 v[200:201], v[164:165], v[164:165], v[200:201]
	v_mul_f32_e32 v224, v165, v165
	v_and_b32_e32 v221, 0xffff0000, v203
	v_lshlrev_b32_e32 v220, 16, v203
	v_pk_add_f32 v[200:201], v[224:225], v[200:201] op_sel_hi:[0,1]
	v_pk_fma_f32 v[200:201], v[220:221], v[220:221], v[200:201]
	v_mul_f32_e32 v224, v221, v221
	s_waitcnt vmcnt(34)
	v_and_b32_e32 v217, 0xffff0000, v205
	v_lshlrev_b32_e32 v216, 16, v205
	v_and_b32_e32 v205, 0xffff0000, v204
	v_lshlrev_b32_e32 v204, 16, v204
	v_pk_add_f32 v[200:201], v[224:225], v[200:201] op_sel_hi:[0,1]
	v_pk_fma_f32 v[200:201], v[204:205], v[204:205], v[200:201]
	v_mul_f32_e32 v224, v205, v205
	v_pk_add_f32 v[200:201], v[224:225], v[200:201] op_sel_hi:[0,1]
	v_pk_fma_f32 v[200:201], v[216:217], v[216:217], v[200:201]
	v_mul_f32_e32 v224, v217, v217
	v_and_b32_e32 v147, 0xffff0000, v167
	v_lshlrev_b32_e32 v146, 16, v167
	v_and_b32_e32 v149, 0xffff0000, v166
	v_lshlrev_b32_e32 v148, 16, v166
	v_and_b32_e32 v167, 0xffff0000, v157
	v_lshlrev_b32_e32 v166, 16, v157
	v_and_b32_e32 v173, 0xffff0000, v156
	v_lshlrev_b32_e32 v172, 16, v156
	v_and_b32_e32 v157, 0xffff0000, v191
	v_lshlrev_b32_e32 v156, 16, v191
	v_and_b32_e32 v161, 0xffff0000, v190
	v_lshlrev_b32_e32 v160, 16, v190
	v_and_b32_e32 v191, 0xffff0000, v175
	v_lshlrev_b32_e32 v190, 16, v175
	v_and_b32_e32 v169, 0xffff0000, v189
	v_lshlrev_b32_e32 v168, 16, v189
	v_and_b32_e32 v193, 0xffff0000, v174
	v_lshlrev_b32_e32 v192, 16, v174
	v_and_b32_e32 v175, 0xffff0000, v188
	v_lshlrev_b32_e32 v174, 16, v188
	v_and_b32_e32 v189, 0xffff0000, v207
	v_lshlrev_b32_e32 v188, 16, v207
	v_and_b32_e32 v207, 0xffff0000, v206
	v_lshlrev_b32_e32 v206, 16, v206
	v_pk_add_f32 v[200:201], v[224:225], v[200:201] op_sel_hi:[0,1]
	v_pk_fma_f32 v[200:201], v[206:207], v[206:207], v[200:201]
	v_mul_f32_e32 v224, v207, v207
	v_pk_add_f32 v[200:201], v[224:225], v[200:201] op_sel_hi:[0,1]
	v_pk_fma_f32 v[200:201], v[188:189], v[188:189], v[200:201]
	v_mul_f32_e32 v224, v189, v189
	v_pk_add_f32 v[200:201], v[224:225], v[200:201] op_sel_hi:[0,1]
	v_pk_fma_f32 v[200:201], v[192:193], v[192:193], v[200:201]
	v_mul_f32_e32 v224, v193, v193
	v_pk_add_f32 v[200:201], v[224:225], v[200:201] op_sel_hi:[0,1]
	v_pk_fma_f32 v[200:201], v[190:191], v[190:191], v[200:201]
	v_mul_f32_e32 v224, v191, v191
	v_pk_add_f32 v[200:201], v[224:225], v[200:201] op_sel_hi:[0,1]
	v_pk_fma_f32 v[200:201], v[182:183], v[182:183], v[200:201]
	v_mul_f32_e32 v224, v183, v183
	v_pk_add_f32 v[200:201], v[224:225], v[200:201] op_sel_hi:[0,1]
	v_pk_fma_f32 v[200:201], v[178:179], v[178:179], v[200:201]
	v_mul_f32_e32 v224, v179, v179
	v_pk_add_f32 v[200:201], v[224:225], v[200:201] op_sel_hi:[0,1]
	v_pk_fma_f32 v[200:201], v[172:173], v[172:173], v[200:201]
	v_mul_f32_e32 v224, v173, v173
	v_pk_add_f32 v[200:201], v[224:225], v[200:201] op_sel_hi:[0,1]
	v_pk_fma_f32 v[200:201], v[166:167], v[166:167], v[200:201]
	v_mul_f32_e32 v224, v167, v167
	v_and_b32_e32 v155, 0xffff0000, v159
	v_lshlrev_b32_e32 v154, 16, v159
	v_and_b32_e32 v159, 0xffff0000, v158
	v_lshlrev_b32_e32 v158, 16, v158
	v_pk_add_f32 v[200:201], v[224:225], v[200:201] op_sel_hi:[0,1]
	v_pk_fma_f32 v[200:201], v[158:159], v[158:159], v[200:201]
	v_mul_f32_e32 v224, v159, v159
	v_pk_add_f32 v[200:201], v[224:225], v[200:201] op_sel_hi:[0,1]
	v_pk_fma_f32 v[200:201], v[154:155], v[154:155], v[200:201]
	v_mul_f32_e32 v224, v155, v155
	s_waitcnt vmcnt(33)
	v_and_b32_e32 v223, 0xffff0000, v211
	v_lshlrev_b32_e32 v222, 16, v211
	v_and_b32_e32 v203, 0xffff0000, v210
	v_lshlrev_b32_e32 v202, 16, v210
	v_and_b32_e32 v211, 0xffff0000, v209
	v_lshlrev_b32_e32 v210, 16, v209
	v_and_b32_e32 v209, 0xffff0000, v208
	v_lshlrev_b32_e32 v208, 16, v208
	v_pk_add_f32 v[200:201], v[224:225], v[200:201] op_sel_hi:[0,1]
	v_pk_fma_f32 v[200:201], v[208:209], v[208:209], v[200:201]
	v_mul_f32_e32 v224, v209, v209
	v_pk_add_f32 v[200:201], v[224:225], v[200:201] op_sel_hi:[0,1]
	v_pk_fma_f32 v[200:201], v[210:211], v[210:211], v[200:201]
	v_mul_f32_e32 v224, v211, v211
	v_pk_add_f32 v[200:201], v[224:225], v[200:201] op_sel_hi:[0,1]
	v_pk_fma_f32 v[200:201], v[202:203], v[202:203], v[200:201]
	v_mul_f32_e32 v224, v203, v203
	v_pk_add_f32 v[200:201], v[224:225], v[200:201] op_sel_hi:[0,1]
	v_pk_fma_f32 v[200:201], v[222:223], v[222:223], v[200:201]
	v_mul_f32_e32 v224, v223, v223
	s_waitcnt vmcnt(32)
	v_and_b32_e32 v219, 0xffff0000, v213
	v_lshlrev_b32_e32 v218, 16, v213
	v_and_b32_e32 v213, 0xffff0000, v212
	v_lshlrev_b32_e32 v212, 16, v212
	v_pk_add_f32 v[200:201], v[224:225], v[200:201] op_sel_hi:[0,1]
	v_pk_fma_f32 v[200:201], v[212:213], v[212:213], v[200:201]
	v_mul_f32_e32 v224, v213, v213
	v_pk_add_f32 v[200:201], v[224:225], v[200:201] op_sel_hi:[0,1]
	v_pk_fma_f32 v[200:201], v[218:219], v[218:219], v[200:201]
	v_mul_f32_e32 v224, v219, v219
	v_and_b32_e32 v181, 0xffff0000, v215
	v_lshlrev_b32_e32 v180, 16, v215
	v_and_b32_e32 v215, 0xffff0000, v214
	v_lshlrev_b32_e32 v214, 16, v214
	v_pk_add_f32 v[200:201], v[224:225], v[200:201] op_sel_hi:[0,1]
	v_pk_fma_f32 v[200:201], v[214:215], v[214:215], v[200:201]
	v_mul_f32_e32 v224, v215, v215
	v_pk_add_f32 v[200:201], v[224:225], v[200:201] op_sel_hi:[0,1]
	v_pk_fma_f32 v[200:201], v[180:181], v[180:181], v[200:201]
	v_mul_f32_e32 v224, v181, v181
	v_pk_add_f32 v[200:201], v[224:225], v[200:201] op_sel_hi:[0,1]
	v_pk_fma_f32 v[200:201], v[174:175], v[174:175], v[200:201]
	v_mul_f32_e32 v224, v175, v175
	v_pk_add_f32 v[200:201], v[224:225], v[200:201] op_sel_hi:[0,1]
	v_pk_fma_f32 v[200:201], v[168:169], v[168:169], v[200:201]
	v_mul_f32_e32 v224, v169, v169
	v_pk_add_f32 v[200:201], v[224:225], v[200:201] op_sel_hi:[0,1]
	v_pk_fma_f32 v[200:201], v[160:161], v[160:161], v[200:201]
	v_mul_f32_e32 v224, v161, v161
	v_pk_add_f32 v[200:201], v[224:225], v[200:201] op_sel_hi:[0,1]
	v_pk_fma_f32 v[200:201], v[156:157], v[156:157], v[200:201]
	v_mul_f32_e32 v224, v157, v157
	v_pk_add_f32 v[200:201], v[224:225], v[200:201] op_sel_hi:[0,1]
	v_pk_fma_f32 v[200:201], v[152:153], v[152:153], v[200:201]
	v_mul_f32_e32 v224, v153, v153
	v_pk_add_f32 v[200:201], v[224:225], v[200:201] op_sel_hi:[0,1]
	v_pk_fma_f32 v[200:201], v[150:151], v[150:151], v[200:201]
	v_mul_f32_e32 v224, v151, v151
	v_pk_add_f32 v[200:201], v[224:225], v[200:201] op_sel_hi:[0,1]
	v_pk_fma_f32 v[200:201], v[148:149], v[148:149], v[200:201]
	v_mul_f32_e32 v224, v149, v149
	v_pk_add_f32 v[200:201], v[224:225], v[200:201] op_sel_hi:[0,1]
	v_pk_fma_f32 v[200:201], v[146:147], v[146:147], v[200:201]
	v_mul_f32_e32 v224, v147, v147
	v_pk_add_f32 v[200:201], v[224:225], v[200:201] op_sel_hi:[0,1]
	v_mov_b32_e32 v187, v200
	s_nop 1
	v_permlane32_swap_b32_e32 v200, v187
	v_add_f32_e32 v187, v200, v187
	v_fmamk_f32 v187, v187, 0x3c000000, v248
	v_mul_f32_e32 v194, 0x4b800000, v187
	v_cmp_gt_f32_e32 vcc, s3, v187
	s_nop 1
	v_cndmask_b32_e32 v187, v187, v194, vcc
	v_rsq_f32_e32 v187, v187
	s_nop 0
	v_mul_f32_e32 v194, 0x45800000, v187
	v_cndmask_b32_e32 v200, v187, v194, vcc
	v_mul_f32_e32 v200, 0x3e0293ee, v200
	s_waitcnt vmcnt(15)
	v_pk_mul_f32 v[142:143], v[142:143], v[200:201] op_sel_hi:[1,0]
	s_waitcnt vmcnt(13)
	v_pk_mul_f32 v[134:135], v[134:135], v[200:201] op_sel_hi:[1,0]
	v_pk_mul_f32 v[176:177], v[142:143], v[176:177]
	v_pk_mul_f32 v[142:143], v[144:145], v[200:201] op_sel_hi:[1,0]
	s_waitcnt vmcnt(12)
	v_pk_mul_f32 v[130:131], v[130:131], v[200:201] op_sel_hi:[1,0]
	v_pk_mul_f32 v[170:171], v[142:143], v[170:171]
	v_pk_mul_f32 v[142:143], v[134:135], v[204:205]
	v_pk_mul_f32 v[134:135], v[136:137], v[200:201] op_sel_hi:[1,0]
	s_waitcnt vmcnt(11)
	v_pk_mul_f32 v[124:125], v[124:125], v[200:201] op_sel_hi:[1,0]
	v_pk_mul_f32 v[136:137], v[134:135], v[216:217]
	v_pk_mul_f32 v[134:135], v[130:131], v[206:207]
	v_pk_mul_f32 v[130:131], v[132:133], v[200:201] op_sel_hi:[1,0]
	s_waitcnt vmcnt(10)
	v_pk_mul_f32 v[120:121], v[120:121], v[200:201] op_sel_hi:[1,0]
	v_pk_mul_f32 v[132:133], v[130:131], v[188:189]
	v_pk_mul_f32 v[130:131], v[124:125], v[192:193]
	v_pk_mul_f32 v[124:125], v[126:127], v[200:201] op_sel_hi:[1,0]
	s_waitcnt vmcnt(9)
	v_pk_mul_f32 v[116:117], v[116:117], v[200:201] op_sel_hi:[1,0]
	v_pk_mul_f32 v[126:127], v[124:125], v[190:191]
	v_pk_mul_f32 v[124:125], v[120:121], v[182:183]
	v_pk_mul_f32 v[120:121], v[122:123], v[200:201] op_sel_hi:[1,0]
	v_pk_mul_f32 v[138:139], v[138:139], v[200:201] op_sel_hi:[1,0]
	v_pk_mul_f32 v[122:123], v[120:121], v[178:179]
	v_pk_mul_f32 v[120:121], v[116:117], v[172:173]
	v_pk_mul_f32 v[116:117], v[118:119], v[200:201] op_sel_hi:[1,0]
	s_waitcnt vmcnt(8)
	v_pk_mul_f32 v[112:113], v[112:113], v[200:201] op_sel_hi:[1,0]
	v_pk_mul_f32 v[164:165], v[138:139], v[164:165]
	v_pk_mul_f32 v[138:139], v[140:141], v[200:201] op_sel_hi:[1,0]
	v_pk_mul_f32 v[118:119], v[116:117], v[166:167]
	v_pk_mul_f32 v[116:117], v[112:113], v[158:159]
	v_pk_mul_f32 v[112:113], v[114:115], v[200:201] op_sel_hi:[1,0]
	s_waitcnt vmcnt(6)
	v_pk_mul_f32 v[108:109], v[200:201], v[108:109] op_sel_hi:[0,1]
	v_pk_mul_f32 v[110:111], v[200:201], v[110:111] op_sel_hi:[0,1]
	v_pk_mul_f32 v[104:105], v[200:201], v[104:105] op_sel_hi:[0,1]
	v_pk_mul_f32 v[106:107], v[200:201], v[106:107] op_sel_hi:[0,1]
	s_waitcnt vmcnt(4)
	v_pk_mul_f32 v[100:101], v[200:201], v[100:101] op_sel_hi:[0,1]
	v_pk_mul_f32 v[102:103], v[200:201], v[102:103] op_sel_hi:[0,1]
	v_pk_mul_f32 v[96:97], v[200:201], v[96:97] op_sel_hi:[0,1]
	v_pk_mul_f32 v[98:99], v[200:201], v[98:99] op_sel_hi:[0,1]
	s_waitcnt vmcnt(2)
	v_pk_mul_f32 v[92:93], v[200:201], v[92:93] op_sel_hi:[0,1]
	v_pk_mul_f32 v[94:95], v[200:201], v[94:95] op_sel_hi:[0,1]
	v_pk_mul_f32 v[88:89], v[200:201], v[88:89] op_sel_hi:[0,1]
	v_pk_mul_f32 v[90:91], v[200:201], v[90:91] op_sel_hi:[0,1]
	s_waitcnt vmcnt(0)
	v_pk_mul_f32 v[84:85], v[200:201], v[84:85] op_sel_hi:[0,1]
	v_pk_mul_f32 v[86:87], v[200:201], v[86:87] op_sel_hi:[0,1]
	v_pk_mul_f32 v[80:81], v[200:201], v[80:81] op_sel_hi:[0,1]
	v_pk_mul_f32 v[82:83], v[200:201], v[82:83] op_sel_hi:[0,1]
	v_pk_mul_f32 v[144:145], v[138:139], v[220:221]
	v_pk_mul_f32 v[112:113], v[112:113], v[154:155]
	v_pk_mul_f32 v[108:109], v[108:109], v[208:209]
	v_pk_mul_f32 v[110:111], v[110:111], v[210:211]
	v_pk_mul_f32 v[104:105], v[104:105], v[202:203]
	v_pk_mul_f32 v[106:107], v[106:107], v[222:223]
	v_pk_mul_f32 v[100:101], v[100:101], v[212:213]
	v_pk_mul_f32 v[102:103], v[102:103], v[218:219]
	v_pk_mul_f32 v[96:97], v[96:97], v[214:215]
	v_pk_mul_f32 v[98:99], v[98:99], v[180:181]
	v_pk_mul_f32 v[92:93], v[92:93], v[174:175]
	v_pk_mul_f32 v[94:95], v[94:95], v[168:169]
	v_pk_mul_f32 v[88:89], v[88:89], v[160:161]
	v_pk_mul_f32 v[90:91], v[90:91], v[156:157]
	v_pk_mul_f32 v[84:85], v[84:85], v[152:153]
	v_pk_mul_f32 v[86:87], v[86:87], v[150:151]
	v_pk_mul_f32 v[80:81], v[80:81], v[148:149]
	v_pk_mul_f32 v[82:83], v[82:83], v[146:147]
	s_cbranch_scc1 .LBB0_880
	v_pk_mul_f32 v[114:115], v[76:77], v[108:109]
	v_pk_mul_f32 v[76:77], v[76:77], v[176:177]
	v_pk_fma_f32 v[114:115], v[72:73], v[176:177], v[114:115] neg_lo:[0,0,1] neg_hi:[0,0,1]
	v_pk_fma_f32 v[108:109], v[72:73], v[108:109], v[76:77]
	v_pk_mul_f32 v[72:73], v[78:79], v[110:111]
	v_pk_mul_f32 v[76:77], v[78:79], v[170:171]
	v_pk_fma_f32 v[72:73], v[74:75], v[170:171], v[72:73] neg_lo:[0,0,1] neg_hi:[0,0,1]
	v_pk_fma_f32 v[110:111], v[74:75], v[110:111], v[76:77]
	v_pk_mul_f32 v[74:75], v[68:69], v[104:105]
	v_mov_b64_e32 v[170:171], v[72:73]
	v_pk_fma_f32 v[74:75], v[60:61], v[164:165], v[74:75] neg_lo:[0,0,1] neg_hi:[0,0,1]
	v_pk_mul_f32 v[60:61], v[60:61], v[104:105]
	v_mov_b64_e32 v[176:177], v[114:115]
	v_pk_fma_f32 v[104:105], v[68:69], v[164:165], v[60:61]
	v_pk_mul_f32 v[60:61], v[70:71], v[106:107]
	v_mov_b64_e32 v[164:165], v[74:75]
	v_pk_fma_f32 v[60:61], v[62:63], v[144:145], v[60:61] neg_lo:[0,0,1] neg_hi:[0,0,1]
	v_pk_mul_f32 v[62:63], v[62:63], v[106:107]
	s_nop 0
	v_pk_fma_f32 v[106:107], v[70:71], v[144:145], v[62:63]
	v_pk_mul_f32 v[62:63], v[64:65], v[100:101]
	v_mov_b64_e32 v[144:145], v[60:61]
	v_pk_fma_f32 v[62:63], v[56:57], v[142:143], v[62:63] neg_lo:[0,0,1] neg_hi:[0,0,1]
	v_pk_mul_f32 v[56:57], v[56:57], v[100:101]
	s_nop 0
	v_pk_fma_f32 v[100:101], v[64:65], v[142:143], v[56:57]
	v_pk_mul_f32 v[56:57], v[66:67], v[102:103]
	v_mov_b64_e32 v[142:143], v[62:63]
	v_pk_fma_f32 v[56:57], v[58:59], v[136:137], v[56:57] neg_lo:[0,0,1] neg_hi:[0,0,1]
	v_pk_mul_f32 v[58:59], v[58:59], v[102:103]
	s_nop 0
	v_pk_fma_f32 v[102:103], v[66:67], v[136:137], v[58:59]
	v_pk_mul_f32 v[58:59], v[52:53], v[96:97]
	v_mov_b64_e32 v[136:137], v[56:57]
	v_pk_fma_f32 v[58:59], v[48:49], v[134:135], v[58:59] neg_lo:[0,0,1] neg_hi:[0,0,1]
	v_pk_mul_f32 v[48:49], v[48:49], v[96:97]
	s_nop 0
	v_pk_fma_f32 v[96:97], v[52:53], v[134:135], v[48:49]
	v_pk_mul_f32 v[48:49], v[54:55], v[98:99]
	v_mov_b64_e32 v[134:135], v[58:59]
	v_pk_fma_f32 v[48:49], v[50:51], v[132:133], v[48:49] neg_lo:[0,0,1] neg_hi:[0,0,1]
	v_pk_mul_f32 v[50:51], v[50:51], v[98:99]
	s_nop 0
	v_pk_fma_f32 v[98:99], v[54:55], v[132:133], v[50:51]
	v_pk_mul_f32 v[50:51], v[44:45], v[92:93]
	v_mov_b64_e32 v[132:133], v[48:49]
	v_pk_fma_f32 v[50:51], v[40:41], v[130:131], v[50:51] neg_lo:[0,0,1] neg_hi:[0,0,1]
	v_pk_mul_f32 v[40:41], v[40:41], v[92:93]
	s_nop 0
	v_pk_fma_f32 v[92:93], v[44:45], v[130:131], v[40:41]
	v_pk_mul_f32 v[40:41], v[46:47], v[94:95]
	v_mov_b64_e32 v[130:131], v[50:51]
	v_pk_fma_f32 v[40:41], v[42:43], v[126:127], v[40:41] neg_lo:[0,0,1] neg_hi:[0,0,1]
	v_pk_mul_f32 v[42:43], v[42:43], v[94:95]
	s_nop 0
	v_pk_fma_f32 v[94:95], v[46:47], v[126:127], v[42:43]
	v_pk_mul_f32 v[42:43], v[36:37], v[88:89]
	v_mov_b64_e32 v[126:127], v[40:41]
	v_pk_fma_f32 v[42:43], v[32:33], v[124:125], v[42:43] neg_lo:[0,0,1] neg_hi:[0,0,1]
	v_pk_mul_f32 v[32:33], v[32:33], v[88:89]
	s_nop 0
	v_pk_fma_f32 v[88:89], v[36:37], v[124:125], v[32:33]
	v_pk_mul_f32 v[32:33], v[38:39], v[90:91]
	v_mov_b64_e32 v[124:125], v[42:43]
	v_pk_fma_f32 v[32:33], v[34:35], v[122:123], v[32:33] neg_lo:[0,0,1] neg_hi:[0,0,1]
	v_pk_mul_f32 v[34:35], v[34:35], v[90:91]
	s_nop 0
	v_pk_fma_f32 v[90:91], v[38:39], v[122:123], v[34:35]
	v_pk_mul_f32 v[34:35], v[28:29], v[84:85]
	v_mov_b64_e32 v[122:123], v[32:33]
	v_pk_fma_f32 v[34:35], v[24:25], v[120:121], v[34:35] neg_lo:[0,0,1] neg_hi:[0,0,1]
	v_pk_mul_f32 v[24:25], v[24:25], v[84:85]
	s_nop 0
	v_pk_fma_f32 v[84:85], v[28:29], v[120:121], v[24:25]
	v_pk_mul_f32 v[24:25], v[30:31], v[86:87]
	v_mov_b64_e32 v[120:121], v[34:35]
	v_pk_fma_f32 v[24:25], v[26:27], v[118:119], v[24:25] neg_lo:[0,0,1] neg_hi:[0,0,1]
	v_pk_mul_f32 v[26:27], v[26:27], v[86:87]
	s_nop 0
	v_pk_fma_f32 v[86:87], v[30:31], v[118:119], v[26:27]
	v_pk_mul_f32 v[26:27], v[20:21], v[80:81]
	v_mov_b64_e32 v[118:119], v[24:25]
	v_pk_fma_f32 v[26:27], v[16:17], v[116:117], v[26:27] neg_lo:[0,0,1] neg_hi:[0,0,1]
	v_pk_mul_f32 v[16:17], v[16:17], v[80:81]
	s_nop 0
	v_pk_fma_f32 v[80:81], v[20:21], v[116:117], v[16:17]
	v_pk_mul_f32 v[16:17], v[22:23], v[82:83]
	v_mov_b64_e32 v[116:117], v[26:27]
	v_pk_fma_f32 v[16:17], v[18:19], v[112:113], v[16:17] neg_lo:[0,0,1] neg_hi:[0,0,1]
	v_pk_mul_f32 v[18:19], v[18:19], v[82:83]
	s_nop 0
	v_pk_fma_f32 v[82:83], v[22:23], v[112:113], v[18:19]
	v_mov_b64_e32 v[112:113], v[16:17]
.LBB0_880:
	v_add_u32_e32 v21, 32, v185
	v_and_b32_e32 v17, 0xfffff0, v185
	v_lshlrev_b32_e32 v18, 1, v185
	v_and_b32_e32 v22, 0xfffff0, v21
	v_lshlrev_b32_e32 v23, 1, v21
	v_and_b32_e32 v16, 63, v184
	v_and_or_b32 v17, v18, 8, v17
	v_and_or_b32 v22, v23, 8, v22
	v_lshrrev_b32_e32 v17, 1, v17
	v_lshrrev_b32_e32 v19, 5, v186
	v_lshrrev_b32_e32 v22, 1, v22
	v_lshlrev_b32_e32 v23, 4, v16
	v_lshrrev_b32_e32 v18, 1, v185
	v_or_b32_e32 v17, v17, v19
	v_and_b32_e32 v20, 3, v185
	v_or_b32_e32 v19, v22, v19
	v_lshlrev_b32_e32 v22, 3, v16
	v_and_b32_e32 v23, 0xc0, v23
	v_lshlrev_b32_e32 v16, 1, v16
	v_and_or_b32 v18, v18, 4, v20
	v_lshlrev_b32_e32 v20, 1, v186
	v_and_or_b32 v23, v22, 24, v23
	v_and_b32_e32 v16, 32, v16
	v_and_b32_e32 v22, 0x100, v22
	v_lshlrev_b32_e32 v17, 9, v17
	v_lshlrev_b32_e32 v18, 6, v18
	v_or3_b32 v114, v23, v16, v22
	v_and_b32_e32 v16, 48, v20
	v_or3_b32 v17, v17, v18, v16
	v_add_u32_e32 v212, 0, v17
	v_lshlrev_b32_e32 v19, 9, v19
	v_cvt_pk_bf16_f32 v138, v176, v177
	v_cvt_pk_bf16_f32 v139, v170, v171
	v_cvt_pk_bf16_f32 v140, v164, v165
	v_cvt_pk_bf16_f32 v141, v144, v145
	v_cvt_pk_bf16_f32 v154, v142, v143
	v_cvt_pk_bf16_f32 v155, v136, v137
	v_cvt_pk_bf16_f32 v156, v134, v135
	v_cvt_pk_bf16_f32 v157, v132, v133
	v_cvt_pk_bf16_f32 v158, v130, v131
	v_cvt_pk_bf16_f32 v159, v126, v127
	v_cvt_pk_bf16_f32 v160, v124, v125
	v_cvt_pk_bf16_f32 v161, v122, v123
	v_cvt_pk_bf16_f32 v150, v120, v121
	v_cvt_pk_bf16_f32 v151, v118, v119
	v_cvt_pk_bf16_f32 v152, v116, v117
	v_cvt_pk_bf16_f32 v153, v112, v113
	v_cvt_pk_bf16_f32 v146, v108, v109
	v_cvt_pk_bf16_f32 v147, v110, v111
	v_cvt_pk_bf16_f32 v148, v104, v105
	v_cvt_pk_bf16_f32 v149, v106, v107
	v_cvt_pk_bf16_f32 v142, v100, v101
	v_cvt_pk_bf16_f32 v143, v102, v103
	v_cvt_pk_bf16_f32 v144, v96, v97
	v_cvt_pk_bf16_f32 v145, v98, v99
	v_cvt_pk_bf16_f32 v134, v92, v93
	v_cvt_pk_bf16_f32 v135, v94, v95
	v_cvt_pk_bf16_f32 v136, v88, v89
	v_cvt_pk_bf16_f32 v137, v90, v91
	v_cvt_pk_bf16_f32 v130, v84, v85
	v_cvt_pk_bf16_f32 v131, v86, v87
	v_cvt_pk_bf16_f32 v132, v80, v81
	v_cvt_pk_bf16_f32 v133, v82, v83
	s_waitcnt vmcnt(0)
	ds_write_b128 v212, v[8:11]
	v_lshlrev_b32_e32 v8, 8, v185
	v_and_b32_e32 v9, 0x70, v184
	v_or3_b32 v16, v19, v18, v16
	v_bitop3_b32 v8, v20, v8, v9 bitop3:0xde
	v_add_u32_e32 v213, 0, v16
	v_add_u32_e32 v214, 0, v8
	ds_write_b128 v213, v[12:15]
	ds_write_b128 v214, v[4:7] offset:32768
	v_lshlrev_b32_e32 v4, 8, v21
	v_bitop3_b32 v4, v20, v4, v9 bitop3:0xde
	v_add_u32_e32 v215, 0, v4
	ds_write_b128 v215, v[0:3] offset:32768
	v_lshlrev_b32_e32 v0, 4, v163
	v_lshlrev_b32_e32 v56, 8, v163
	v_and_b32_e32 v57, 0x70, v0
	v_bitop3_b32 v0, v162, v56, v57 bitop3:0xde
	v_add_u32_e32 v216, 0, v0
	s_waitcnt lgkmcnt(0)
	s_barrier
	ds_read_b128 v[16:19], v216 offset:32768
	ds_read_b128 v[20:23], v216 offset:40960
	s_waitcnt lgkmcnt(1)
	v_mfma_f32_32x32x16_bf16 v[32:47], v[16:19], v[138:141], 0
	v_or_b32_e32 v48, 32, v162
	v_bitop3_b32 v48, v48, v56, v57 bitop3:0xde
	v_add_u32_e32 v218, 0, v48
	ds_read_b128 v[48:51], v218 offset:32768
	ds_read_b128 v[52:55], v218 offset:40960
	s_cmp_lg_u32 0, -1
	s_cselect_b32 s53, 0, 0
	s_add_u32 s16, s10, s96
	s_waitcnt lgkmcnt(2)
	v_mfma_f32_32x32x16_bf16 v[16:31], v[20:23], v[138:141], 0
	s_addc_u32 s17, s11, s97
	v_mov_b32_e32 v199, v129
	s_add_u32 s18, s8, s96
	s_addc_u32 s19, s9, s97
	v_lshl_add_u64 v[60:61], s[18:19], 0, v[198:199]
	s_add_u32 s2, s16, s96
	s_addc_u32 s3, s17, s97
	s_waitcnt lgkmcnt(1)
	v_mfma_f32_32x32x16_bf16 v[32:47], v[48:51], v[154:157], v[32:47]
	v_or_b32_e32 v48, 64, v162
	v_bitop3_b32 v48, v48, v56, v57 bitop3:0xde
	v_add_u32_e32 v219, 0, v48
	v_lshl_add_u64 v[64:65], s[2:3], 0, v[128:129]
	s_mov_b32 s72, s73
	s_mov_b32 s74, s73
	s_mov_b32 s75, s73
	s_waitcnt lgkmcnt(0)
	v_mfma_f32_32x32x16_bf16 v[16:31], v[52:55], v[154:157], v[16:31]
	ds_read_b128 v[48:51], v219 offset:32768
	ds_read_b128 v[52:55], v219 offset:40960
	s_mov_b32 s76, s73
	s_mov_b32 s77, s73
	s_mov_b32 s78, s73
	s_mov_b32 s79, s73
	s_mov_b32 s80, s73
	s_mov_b32 s81, s73
	s_waitcnt lgkmcnt(1)
	v_mfma_f32_32x32x16_bf16 v[32:47], v[48:51], v[158:161], v[32:47]
	v_or_b32_e32 v48, 0x60, v162
	v_bitop3_b32 v48, v48, v56, v57 bitop3:0xde
	v_add_u32_e32 v220, 0, v48
	s_mov_b32 s82, s73
	s_mov_b32 s83, s73
	s_mov_b32 s84, s73
	s_mov_b32 s85, s73
	s_waitcnt lgkmcnt(0)
	v_mfma_f32_32x32x16_bf16 v[16:31], v[52:55], v[158:161], v[16:31]
	ds_read_b128 v[48:51], v220 offset:32768
	ds_read_b128 v[52:55], v220 offset:40960
	s_mov_b32 s86, s73
	s_mov_b32 s87, s73
	v_mov_b64_e32 v[0:1], s[72:73]
	v_mov_b64_e32 v[14:15], s[86:87]
	v_add_u32_e32 v209, s53, v114
	v_mov_b64_e32 v[2:3], s[74:75]
	s_waitcnt lgkmcnt(1)
	v_mfma_f32_32x32x16_bf16 v[32:47], v[48:51], v[150:153], v[32:47]
	v_or_b32_e32 v48, 0x80, v162
	v_bitop3_b32 v48, v48, v56, v57 bitop3:0xde
	v_add_u32_e32 v221, 0, v48
	v_mov_b64_e32 v[4:5], s[76:77]
	v_mov_b64_e32 v[6:7], s[78:79]
	v_mov_b64_e32 v[8:9], s[80:81]
	v_mov_b64_e32 v[10:11], s[82:83]
	s_waitcnt lgkmcnt(0)
	v_mfma_f32_32x32x16_bf16 v[16:31], v[52:55], v[150:153], v[16:31]
	ds_read_b128 v[48:51], v221 offset:32768
	ds_read_b128 v[52:55], v221 offset:40960
	v_mov_b64_e32 v[12:13], s[84:85]
	s_mov_b32 s39, 4
	v_mov_b32_e32 v217, 0
	v_readlane_b32 s80, v255, 48
	s_movk_i32 s79, 0xff
	s_movk_i32 s84, 0xffe0
	s_waitcnt lgkmcnt(1)
	v_mfma_f32_32x32x16_bf16 v[32:47], v[48:51], v[146:149], v[32:47]
	v_or_b32_e32 v48, 0xa0, v162
	v_bitop3_b32 v48, v48, v56, v57 bitop3:0xde
	v_add_u32_e32 v222, 0, v48
	s_waitcnt lgkmcnt(0)
	v_mfma_f32_32x32x16_bf16 v[16:31], v[52:55], v[146:149], v[16:31]
	ds_read_b128 v[48:51], v222 offset:32768
	ds_read_b128 v[52:55], v222 offset:40960
	s_waitcnt lgkmcnt(1)
	v_mfma_f32_32x32x16_bf16 v[32:47], v[48:51], v[142:145], v[32:47]
	v_or_b32_e32 v48, 0xc0, v162
	v_bitop3_b32 v48, v48, v56, v57 bitop3:0xde
	v_add_u32_e32 v224, 0, v48
	s_waitcnt lgkmcnt(0)
	v_mfma_f32_32x32x16_bf16 v[16:31], v[52:55], v[142:145], v[16:31]
	ds_read_b128 v[48:51], v224 offset:32768
	ds_read_b128 v[52:55], v224 offset:40960
	s_waitcnt lgkmcnt(1)
	v_mfma_f32_32x32x16_bf16 v[32:47], v[48:51], v[134:137], v[32:47]
	v_or_b32_e32 v48, 0xe0, v162
	v_bitop3_b32 v48, v48, v56, v57 bitop3:0xde
	v_add_u32_e32 v223, 0, v48
	v_lshl_add_u64 v[56:57], s[18:19], 0, v[128:129]
	s_waitcnt lgkmcnt(0)
	v_mfma_f32_32x32x16_bf16 v[16:31], v[52:55], v[134:137], v[16:31]
	ds_read_b128 v[48:51], v223 offset:32768
	ds_read_b128 v[52:55], v223 offset:40960
	global_load_dwordx4 v[56:59], v[56:57], off
	s_nop 0
	global_load_dwordx4 v[60:63], v[60:61], off
	s_nop 0
	global_load_dwordx4 v[162:165], v[64:65], off
	v_lshl_add_u64 v[64:65], s[2:3], 0, v[198:199]
	s_waitcnt lgkmcnt(1)
	v_mfma_f32_32x32x16_bf16 v[32:47], v[48:51], v[130:133], v[32:47]
	global_load_dwordx4 v[166:169], v[64:65], off
	s_waitcnt lgkmcnt(0)
	v_mfma_f32_32x32x16_bf16 v[16:31], v[52:55], v[130:133], v[16:31]
	s_nop 8
	v_lshl_add_u64 v[48:49], s[16:17], 0, v[128:129]
	global_load_dwordx4 v[48:51], v[48:49], off
	v_lshl_add_u64 v[52:53], s[16:17], 0, v[198:199]
	global_load_dwordx4 v[52:55], v[52:53], off
	s_add_u32 s16, s18, s96
	s_addc_u32 s17, s19, s97
	v_lshl_add_u64 v[64:65], s[16:17], 0, v[128:129]
	global_load_dwordx4 v[170:173], v[64:65], off
	v_lshl_add_u64 v[64:65], s[16:17], 0, v[198:199]
	global_load_dwordx4 v[174:177], v[64:65], off
	s_and_b64 s[2:3], s[14:15], exec
	s_cselect_b32 s14, 3, 35
	s_waitcnt vmcnt(4)
	s_waitcnt vmcnt(3)
	ds_write_b128 v212, v[48:51] offset:16384
	s_waitcnt vmcnt(2)
	ds_write_b128 v213, v[52:55] offset:16384
	ds_write_b128 v214, v[56:59] offset:49152
	ds_write_b128 v215, v[60:63] offset:49152
	v_exp_f32_e32 v64, v32
	v_exp_f32_e32 v65, v33
	v_exp_f32_e32 v66, v34
	v_exp_f32_e32 v67, v35
	v_exp_f32_e32 v68, v36
	v_exp_f32_e32 v69, v37
	v_exp_f32_e32 v70, v38
	v_exp_f32_e32 v71, v39
	v_exp_f32_e32 v72, v40
	v_exp_f32_e32 v73, v41
	v_exp_f32_e32 v74, v42
	v_exp_f32_e32 v80, v16
	v_exp_f32_e32 v81, v17
	v_exp_f32_e32 v75, v43
	v_exp_f32_e32 v76, v44
	v_exp_f32_e32 v77, v45
	v_exp_f32_e32 v78, v46
	v_exp_f32_e32 v79, v47
	v_exp_f32_e32 v82, v18
	v_exp_f32_e32 v83, v19
	v_lshl_add_u64 v[16:17], s[12:13], 0, v[128:129]
	v_lshl_add_u64 v[18:19], s[12:13], 0, v[198:199]
	v_exp_f32_e32 v94, v30
	v_exp_f32_e32 v95, v31
	v_exp_f32_e32 v92, v28
	v_exp_f32_e32 v93, v29
	v_exp_f32_e32 v196, v26
	v_exp_f32_e32 v197, v27
	v_exp_f32_e32 v194, v24
	v_exp_f32_e32 v195, v25
	v_exp_f32_e32 v86, v22
	v_exp_f32_e32 v87, v23
	v_exp_f32_e32 v84, v20
	v_exp_f32_e32 v85, v21
	s_addk_i32 s53, 0x4000
	v_lshl_add_u64 v[200:201], s[64:65], 0, v[16:17]
	v_lshl_add_u64 v[202:203], s[64:65], 0, v[18:19]
	v_lshl_add_u64 v[204:205], s[66:67], 0, v[16:17]
	v_lshl_add_u64 v[206:207], s[66:67], 0, v[18:19]
	v_mov_b64_e32 v[62:63], v[14:15]
	v_mov_b64_e32 v[46:47], v[14:15]
	v_mov_b64_e32 v[30:31], v[14:15]
	v_add_u32_e32 v211, s53, v114
	v_mov_b64_e32 v[60:61], v[12:13]
	v_mov_b64_e32 v[58:59], v[10:11]
	v_mov_b64_e32 v[56:57], v[8:9]
	v_mov_b64_e32 v[54:55], v[6:7]
	v_mov_b64_e32 v[52:53], v[4:5]
	v_mov_b64_e32 v[50:51], v[2:3]
	v_mov_b64_e32 v[48:49], v[0:1]
	v_mov_b64_e32 v[44:45], v[12:13]
	v_mov_b64_e32 v[42:43], v[10:11]
	v_mov_b64_e32 v[40:41], v[8:9]
	v_mov_b64_e32 v[38:39], v[6:7]
	v_mov_b64_e32 v[36:37], v[4:5]
	v_mov_b64_e32 v[34:35], v[2:3]
	v_mov_b64_e32 v[32:33], v[0:1]
	v_mov_b64_e32 v[28:29], v[12:13]
	v_mov_b64_e32 v[26:27], v[10:11]
	v_mov_b64_e32 v[24:25], v[8:9]
	v_mov_b64_e32 v[22:23], v[6:7]
	v_mov_b64_e32 v[20:21], v[4:5]
	v_mov_b64_e32 v[18:19], v[2:3]
	v_mov_b64_e32 v[16:17], v[0:1]
	s_mov_b32 s53, 0x38e38e39
	s_waitcnt lgkmcnt(0)
	s_barrier
.LBB0_881:
	ds_read_b128 v[96:99], v216 offset:49152
	ds_read_b128 v[100:103], v216 offset:57344
	ds_read_b128 v[178:181], v218 offset:49152
	ds_read_b128 v[182:185], v218 offset:57344
	s_waitcnt lgkmcnt(3)
	v_mfma_f32_32x32x16_bf16 v[112:127], v[96:99], v[138:141], 0
	s_waitcnt lgkmcnt(2)
	v_mfma_f32_32x32x16_bf16 v[96:111], v[100:103], v[138:141], 0
	s_waitcnt lgkmcnt(1)
	v_mfma_f32_32x32x16_bf16 v[112:127], v[178:181], v[154:157], v[112:127]
	s_waitcnt lgkmcnt(0)
	v_mfma_f32_32x32x16_bf16 v[96:111], v[182:185], v[154:157], v[96:111]
	ds_read_b128 v[178:181], v219 offset:49152
	ds_read_b128 v[182:185], v219 offset:57344
	s_waitcnt lgkmcnt(1)
	v_mfma_f32_32x32x16_bf16 v[112:127], v[178:181], v[158:161], v[112:127]
	s_waitcnt lgkmcnt(0)
	v_mfma_f32_32x32x16_bf16 v[96:111], v[182:185], v[158:161], v[96:111]
	ds_read_b128 v[178:181], v220 offset:49152
	ds_read_b128 v[182:185], v220 offset:57344
	s_waitcnt lgkmcnt(1)
	v_mfma_f32_32x32x16_bf16 v[112:127], v[178:181], v[150:153], v[112:127]
	s_waitcnt lgkmcnt(0)
	v_mfma_f32_32x32x16_bf16 v[96:111], v[182:185], v[150:153], v[96:111]
	ds_read_b128 v[178:181], v221 offset:49152
	ds_read_b128 v[182:185], v221 offset:57344
	s_waitcnt lgkmcnt(1)
	v_mfma_f32_32x32x16_bf16 v[112:127], v[178:181], v[146:149], v[112:127]
	s_waitcnt lgkmcnt(0)
	v_mfma_f32_32x32x16_bf16 v[96:111], v[182:185], v[146:149], v[96:111]
	ds_read_b128 v[178:181], v222 offset:49152
	ds_read_b128 v[182:185], v222 offset:57344
	s_waitcnt lgkmcnt(1)
	v_mfma_f32_32x32x16_bf16 v[112:127], v[178:181], v[142:145], v[112:127]
	s_waitcnt lgkmcnt(0)
	v_mfma_f32_32x32x16_bf16 v[96:111], v[182:185], v[142:145], v[96:111]
	ds_read_b128 v[178:181], v224 offset:49152
	ds_read_b128 v[182:185], v224 offset:57344
	s_waitcnt lgkmcnt(1)
	v_mfma_f32_32x32x16_bf16 v[112:127], v[178:181], v[134:137], v[112:127]
	s_waitcnt lgkmcnt(0)
	v_mfma_f32_32x32x16_bf16 v[96:111], v[182:185], v[134:137], v[96:111]
	ds_read_b128 v[178:181], v223 offset:49152
	ds_read_b128 v[182:185], v223 offset:57344
	s_waitcnt lgkmcnt(1)
	v_mfma_f32_32x32x16_bf16 v[112:127], v[178:181], v[130:133], v[112:127]
	v_add_f32_e32 v88, v64, v65
	v_add_f32_e32 v89, v72, v73
	v_add_f32_e32 v90, v80, v81
	v_add_f32_e32 v91, v194, v195
	v_add_f32_e32 v88, v66, v88
	v_add_f32_e32 v89, v74, v89
	v_add_f32_e32 v90, v82, v90
	v_add_f32_e32 v91, v196, v91
	v_add_f32_e32 v88, v67, v88
	v_add_f32_e32 v89, v75, v89
	v_add_f32_e32 v90, v83, v90
	v_add_f32_e32 v91, v197, v91
	v_add_f32_e32 v88, v68, v88
	v_add_f32_e32 v89, v76, v89
	v_add_f32_e32 v90, v84, v90
	v_add_f32_e32 v91, v92, v91
	v_add_f32_e32 v88, v69, v88
	v_add_f32_e32 v89, v77, v89
	v_add_f32_e32 v90, v85, v90
	v_add_f32_e32 v91, v93, v91
	v_add_f32_e32 v88, v70, v88
	v_add_f32_e32 v89, v78, v89
	v_add_f32_e32 v90, v86, v90
	v_add_f32_e32 v91, v94, v91
	v_add_f32_e32 v88, v71, v88
	v_add_f32_e32 v89, v79, v89
	v_add_f32_e32 v90, v87, v90
	v_add_f32_e32 v91, v95, v91
	v_add_f32_e32 v88, v89, v88
	v_add_f32_e32 v89, v91, v90
	v_add_f32_e32 v227, v88, v89
	v_mov_b32_e32 v228, v227
	v_cvt_pk_bf16_f32 v88, v64, v65
	v_cvt_pk_bf16_f32 v89, v66, v67
	v_cvt_pk_bf16_f32 v90, v68, v69
	v_cvt_pk_bf16_f32 v91, v70, v71
	s_nop 1
	v_permlane32_swap_b32_e32 v227, v228
	v_permlane32_swap_b32_e32 v88, v90
	v_permlane32_swap_b32_e32 v89, v91
	v_cvt_pk_bf16_f32 v72, v72, v73
	v_cvt_pk_bf16_f32 v73, v74, v75
	v_cvt_pk_bf16_f32 v74, v76, v77
	v_cvt_pk_bf16_f32 v75, v78, v79
	v_cvt_pk_bf16_f32 v64, v80, v81
	v_cvt_pk_bf16_f32 v65, v82, v83
	v_cvt_pk_bf16_f32 v66, v84, v85
	v_cvt_pk_bf16_f32 v67, v86, v87
	v_cvt_pk_bf16_f32 v68, v194, v195
	v_cvt_pk_bf16_f32 v69, v196, v197
	v_cvt_pk_bf16_f32 v70, v92, v93
	v_cvt_pk_bf16_f32 v71, v94, v95
	s_waitcnt lgkmcnt(0)
	v_mfma_f32_32x32x16_bf16 v[96:111], v[182:185], v[130:133], v[96:111]
	v_permlane32_swap_b32_e32 v72, v74
	v_permlane32_swap_b32_e32 v73, v75
	v_permlane32_swap_b32_e32 v64, v66
	v_permlane32_swap_b32_e32 v65, v67
	v_permlane32_swap_b32_e32 v68, v70
	v_permlane32_swap_b32_e32 v69, v71
	s_add_i32 s2, s39, -1
	s_mul_i32 s2, s2, s62
	s_lshl_b32 s72, s2, 6
	s_lshl_b64 s[2:3], s[72:73], 1
	s_add_u32 s12, s10, s2
	s_addc_u32 s13, s11, s3
	s_add_u32 s2, s8, s2
	s_addc_u32 s3, s9, s3
	global_load_dwordx4 v[178:181], v128, s[12:13]
	global_load_dwordx4 v[182:185], v198, s[12:13]
	global_load_dwordx4 v[186:189], v128, s[2:3]
	global_load_dwordx4 v[190:193], v198, s[2:3]
	ds_read_b64_tr_b16 v[76:77], v209 offset:0
	ds_read_b64_tr_b16 v[78:79], v209 offset:0x800
	ds_read_b64_tr_b16 v[80:81], v209 offset:0x1000
	ds_read_b64_tr_b16 v[82:83], v209 offset:0x1800
	ds_read_b64_tr_b16 v[84:85], v209 offset:0x2000
	ds_read_b64_tr_b16 v[86:87], v209 offset:0x2800
	ds_read_b64_tr_b16 v[92:93], v209 offset:0x3000
	ds_read_b64_tr_b16 v[94:95], v209 offset:0x3800
	s_waitcnt lgkmcnt(0)
	s_nop 0
	v_mfma_f32_32x32x16_bf16 v[0:15], v[76:79], v[88:91], v[0:15]
	v_mfma_f32_32x32x16_bf16 v[0:15], v[80:83], v[72:75], v[0:15]
	v_mfma_f32_32x32x16_bf16 v[0:15], v[84:87], v[64:67], v[0:15]
	ds_read_b64_tr_b16 v[76:77], v209 offset:0x200
	ds_read_b64_tr_b16 v[78:79], v209 offset:0xa00
	ds_read_b64_tr_b16 v[80:81], v209 offset:0x1200
	v_mfma_f32_32x32x16_bf16 v[0:15], v[92:95], v[68:71], v[0:15]
	ds_read_b64_tr_b16 v[82:83], v209 offset:0x1a00
	ds_read_b64_tr_b16 v[84:85], v209 offset:0x2200
	ds_read_b64_tr_b16 v[86:87], v209 offset:0x2a00
	ds_read_b64_tr_b16 v[92:93], v209 offset:0x3200
	ds_read_b64_tr_b16 v[94:95], v209 offset:0x3a00
	s_waitcnt lgkmcnt(0)
	v_mfma_f32_32x32x16_bf16 v[48:63], v[76:79], v[88:91], v[48:63]
	v_mfma_f32_32x32x16_bf16 v[48:63], v[80:83], v[72:75], v[48:63]
	v_mfma_f32_32x32x16_bf16 v[48:63], v[84:87], v[64:67], v[48:63]
	ds_read_b64_tr_b16 v[76:77], v209 offset:0x400
	ds_read_b64_tr_b16 v[78:79], v209 offset:0xc00
	ds_read_b64_tr_b16 v[80:81], v209 offset:0x1400
	ds_read_b64_tr_b16 v[82:83], v209 offset:0x1c00
	v_mfma_f32_32x32x16_bf16 v[48:63], v[92:95], v[68:71], v[48:63]
	ds_read_b64_tr_b16 v[84:85], v209 offset:0x2400
	ds_read_b64_tr_b16 v[86:87], v209 offset:0x2c00
	ds_read_b64_tr_b16 v[92:93], v209 offset:0x3400
	ds_read_b64_tr_b16 v[94:95], v209 offset:0x3c00
	s_waitcnt lgkmcnt(0)
	v_mfma_f32_32x32x16_bf16 v[32:47], v[76:79], v[88:91], v[32:47]
	ds_read_b64_tr_b16 v[76:77], v209 offset:0x600
	ds_read_b64_tr_b16 v[78:79], v209 offset:0xe00
	v_exp_f32_e32 v234, v104
	v_exp_f32_e32 v235, v105
	v_exp_f32_e32 v236, v106
	v_exp_f32_e32 v237, v107
	v_exp_f32_e32 v238, v108
	v_exp_f32_e32 v239, v109
	v_exp_f32_e32 v240, v110
	v_exp_f32_e32 v241, v111
	v_mfma_f32_32x32x16_bf16 v[32:47], v[80:83], v[72:75], v[32:47]
	v_exp_f32_e32 v80, v112
	v_exp_f32_e32 v81, v113
	v_exp_f32_e32 v82, v114
	v_exp_f32_e32 v83, v115
	v_mfma_f32_32x32x16_bf16 v[32:47], v[84:87], v[64:67], v[32:47]
	v_exp_f32_e32 v84, v116
	v_exp_f32_e32 v85, v117
	v_exp_f32_e32 v86, v118
	v_exp_f32_e32 v87, v119
	v_exp_f32_e32 v112, v96
	v_exp_f32_e32 v113, v97
	v_exp_f32_e32 v114, v98
	v_exp_f32_e32 v115, v99
	v_exp_f32_e32 v116, v100
	v_exp_f32_e32 v117, v101
	v_exp_f32_e32 v118, v102
	v_exp_f32_e32 v119, v103
	v_mfma_f32_32x32x16_bf16 v[32:47], v[92:95], v[68:71], v[32:47]
	ds_read_b64_tr_b16 v[92:93], v209 offset:0x1600
	ds_read_b64_tr_b16 v[94:95], v209 offset:0x1e00
	ds_read_b64_tr_b16 v[96:97], v209 offset:0x2600
	ds_read_b64_tr_b16 v[98:99], v209 offset:0x2e00
	ds_read_b64_tr_b16 v[100:101], v209 offset:0x3600
	ds_read_b64_tr_b16 v[102:103], v209 offset:0x3e00
	s_waitcnt lgkmcnt(0)
	v_mfma_f32_32x32x16_bf16 v[16:31], v[76:79], v[88:91], v[16:31]
	v_exp_f32_e32 v88, v120
	v_exp_f32_e32 v89, v121
	v_exp_f32_e32 v90, v122
	v_exp_f32_e32 v91, v123
	v_mfma_f32_32x32x16_bf16 v[16:31], v[92:95], v[72:75], v[16:31]
	v_exp_f32_e32 v92, v124
	v_exp_f32_e32 v93, v125
	v_exp_f32_e32 v94, v126
	v_exp_f32_e32 v95, v127
	s_barrier
	v_mfma_f32_32x32x16_bf16 v[16:31], v[96:99], v[64:67], v[16:31]
	s_waitcnt vmcnt(4)
	s_waitcnt vmcnt(7)
	ds_write_b128 v212, v[162:165]
	s_waitcnt vmcnt(6)
	ds_write_b128 v213, v[166:169]
	s_waitcnt vmcnt(5)
	ds_write_b128 v214, v[170:173] offset:32768
	s_waitcnt vmcnt(4)
	ds_write_b128 v215, v[174:177] offset:32768
	v_mfma_f32_32x32x16_bf16 v[16:31], v[100:103], v[68:71], v[16:31]
.LBB0_883:
	s_waitcnt lgkmcnt(0)
	s_barrier
	ds_read_b128 v[64:67], v216 offset:32768
	ds_read_b128 v[68:71], v216 offset:40960
	ds_read_b128 v[162:165], v218 offset:32768
	ds_read_b128 v[166:169], v218 offset:40960
	s_waitcnt lgkmcnt(3)
	v_mfma_f32_32x32x16_bf16 v[96:111], v[64:67], v[138:141], 0
	s_waitcnt lgkmcnt(2)
	v_mfma_f32_32x32x16_bf16 v[64:79], v[68:71], v[138:141], 0
	s_waitcnt lgkmcnt(1)
	v_mfma_f32_32x32x16_bf16 v[96:111], v[162:165], v[154:157], v[96:111]
	s_waitcnt lgkmcnt(0)
	v_mfma_f32_32x32x16_bf16 v[64:79], v[166:169], v[154:157], v[64:79]
	ds_read_b128 v[162:165], v219 offset:32768
	ds_read_b128 v[166:169], v219 offset:40960
	s_waitcnt lgkmcnt(1)
	v_mfma_f32_32x32x16_bf16 v[96:111], v[162:165], v[158:161], v[96:111]
	s_waitcnt lgkmcnt(0)
	v_mfma_f32_32x32x16_bf16 v[64:79], v[166:169], v[158:161], v[64:79]
	ds_read_b128 v[162:165], v220 offset:32768
	ds_read_b128 v[166:169], v220 offset:40960
	s_waitcnt lgkmcnt(1)
	v_mfma_f32_32x32x16_bf16 v[96:111], v[162:165], v[150:153], v[96:111]
	s_waitcnt lgkmcnt(0)
	v_mfma_f32_32x32x16_bf16 v[64:79], v[166:169], v[150:153], v[64:79]
	ds_read_b128 v[162:165], v221 offset:32768
	ds_read_b128 v[166:169], v221 offset:40960
	s_waitcnt lgkmcnt(1)
	v_mfma_f32_32x32x16_bf16 v[96:111], v[162:165], v[146:149], v[96:111]
	s_waitcnt lgkmcnt(0)
	v_mfma_f32_32x32x16_bf16 v[64:79], v[166:169], v[146:149], v[64:79]
	ds_read_b128 v[162:165], v222 offset:32768
	ds_read_b128 v[166:169], v222 offset:40960
	s_waitcnt lgkmcnt(1)
	v_mfma_f32_32x32x16_bf16 v[96:111], v[162:165], v[142:145], v[96:111]
	s_waitcnt lgkmcnt(0)
	v_mfma_f32_32x32x16_bf16 v[64:79], v[166:169], v[142:145], v[64:79]
	ds_read_b128 v[162:165], v224 offset:32768
	ds_read_b128 v[166:169], v224 offset:40960
	s_waitcnt lgkmcnt(1)
	v_mfma_f32_32x32x16_bf16 v[96:111], v[162:165], v[134:137], v[96:111]
	s_waitcnt lgkmcnt(0)
	v_mfma_f32_32x32x16_bf16 v[64:79], v[166:169], v[134:137], v[64:79]
	ds_read_b128 v[162:165], v223 offset:32768
	ds_read_b128 v[166:169], v223 offset:40960
	s_waitcnt lgkmcnt(1)
	v_mfma_f32_32x32x16_bf16 v[96:111], v[162:165], v[130:133], v[96:111]
	v_add_f32_e32 v120, v80, v81
	v_add_f32_e32 v121, v88, v89
	v_add_f32_e32 v122, v112, v113
	s_waitcnt lgkmcnt(0)
	v_mfma_f32_32x32x16_bf16 v[64:79], v[166:169], v[130:133], v[64:79]
	v_add_f32_e32 v123, v234, v235
	v_add_f32_e32 v120, v82, v120
	v_add_f32_e32 v121, v90, v121
	v_add_f32_e32 v122, v114, v122
	v_add_f32_e32 v123, v236, v123
	v_add_f32_e32 v120, v83, v120
	v_add_f32_e32 v121, v91, v121
	v_add_f32_e32 v122, v115, v122
	v_add_f32_e32 v123, v237, v123
	v_add_f32_e32 v120, v84, v120
	v_add_f32_e32 v121, v92, v121
	v_add_f32_e32 v122, v116, v122
	v_add_f32_e32 v123, v238, v123
	v_add_f32_e32 v120, v85, v120
	v_add_f32_e32 v121, v93, v121
	v_add_f32_e32 v122, v117, v122
	v_add_f32_e32 v123, v239, v123
	v_add_f32_e32 v120, v86, v120
	v_add_f32_e32 v121, v94, v121
	v_add_f32_e32 v122, v118, v122
	v_add_f32_e32 v123, v240, v123
	v_add_f32_e32 v120, v87, v120
	v_add_f32_e32 v121, v95, v121
	v_add_f32_e32 v122, v119, v122
	v_add_f32_e32 v123, v241, v123
	v_add_f32_e32 v120, v121, v120
	v_add_f32_e32 v121, v123, v122
	v_add_f32_e32 v229, v120, v121
	v_mov_b32_e32 v233, v229
	s_nop 1
	v_permlane32_swap_b32_e32 v229, v233
	v_cvt_pk_bf16_f32 v124, v80, v81
	v_cvt_pk_bf16_f32 v125, v82, v83
	v_cvt_pk_bf16_f32 v126, v84, v85
	v_cvt_pk_bf16_f32 v127, v86, v87
	v_cvt_pk_bf16_f32 v120, v88, v89
	v_cvt_pk_bf16_f32 v121, v90, v91
	v_cvt_pk_bf16_f32 v122, v92, v93
	v_cvt_pk_bf16_f32 v123, v94, v95
	v_cvt_pk_bf16_f32 v112, v112, v113
	v_cvt_pk_bf16_f32 v113, v114, v115
	v_cvt_pk_bf16_f32 v114, v116, v117
	v_cvt_pk_bf16_f32 v115, v118, v119
	v_cvt_pk_bf16_f32 v116, v234, v235
	v_cvt_pk_bf16_f32 v117, v236, v237
	v_cvt_pk_bf16_f32 v118, v238, v239
	v_cvt_pk_bf16_f32 v119, v240, v241
	s_nop 0
	v_permlane32_swap_b32_e32 v124, v126
	v_permlane32_swap_b32_e32 v125, v127
	v_permlane32_swap_b32_e32 v120, v122
	v_permlane32_swap_b32_e32 v121, v123
	v_permlane32_swap_b32_e32 v112, v114
	v_permlane32_swap_b32_e32 v113, v115
	v_permlane32_swap_b32_e32 v116, v118
	v_permlane32_swap_b32_e32 v117, v119
	s_min_i32 s2, s39, s14
	s_mul_i32 s2, s2, s62
	s_lshl_b32 s72, s2, 6
	s_lshl_b64 s[2:3], s[72:73], 1
	s_add_u32 s12, s10, s2
	s_addc_u32 s13, s11, s3
	s_add_u32 s2, s8, s2
	s_addc_u32 s3, s9, s3
	global_load_dwordx4 v[162:165], v128, s[12:13]
	global_load_dwordx4 v[166:169], v198, s[12:13]
	global_load_dwordx4 v[170:173], v128, s[2:3]
	global_load_dwordx4 v[174:177], v198, s[2:3]
	ds_read_b64_tr_b16 v[80:81], v211 offset:0
	ds_read_b64_tr_b16 v[82:83], v211 offset:0x800
	ds_read_b64_tr_b16 v[84:85], v211 offset:0x1000
	ds_read_b64_tr_b16 v[86:87], v211 offset:0x1800
	ds_read_b64_tr_b16 v[88:89], v211 offset:0x2000
	ds_read_b64_tr_b16 v[90:91], v211 offset:0x2800
	ds_read_b64_tr_b16 v[92:93], v211 offset:0x3000
	ds_read_b64_tr_b16 v[94:95], v211 offset:0x3800
	s_waitcnt lgkmcnt(0)
	s_nop 0
	v_mfma_f32_32x32x16_bf16 v[0:15], v[80:83], v[124:127], v[0:15]
	v_mfma_f32_32x32x16_bf16 v[0:15], v[84:87], v[120:123], v[0:15]
	v_mfma_f32_32x32x16_bf16 v[0:15], v[88:91], v[112:115], v[0:15]
	ds_read_b64_tr_b16 v[80:81], v211 offset:0x200
	ds_read_b64_tr_b16 v[82:83], v211 offset:0xa00
	ds_read_b64_tr_b16 v[84:85], v211 offset:0x1200
	v_mfma_f32_32x32x16_bf16 v[0:15], v[92:95], v[116:119], v[0:15]
	ds_read_b64_tr_b16 v[86:87], v211 offset:0x1a00
	ds_read_b64_tr_b16 v[88:89], v211 offset:0x2200
	ds_read_b64_tr_b16 v[90:91], v211 offset:0x2a00
	ds_read_b64_tr_b16 v[92:93], v211 offset:0x3200
	ds_read_b64_tr_b16 v[94:95], v211 offset:0x3a00
	s_waitcnt lgkmcnt(0)
	v_mfma_f32_32x32x16_bf16 v[48:63], v[80:83], v[124:127], v[48:63]
	v_mfma_f32_32x32x16_bf16 v[48:63], v[84:87], v[120:123], v[48:63]
	v_mfma_f32_32x32x16_bf16 v[48:63], v[88:91], v[112:115], v[48:63]
	ds_read_b64_tr_b16 v[80:81], v211 offset:0x400
	ds_read_b64_tr_b16 v[82:83], v211 offset:0xc00
	ds_read_b64_tr_b16 v[84:85], v211 offset:0x1400
	ds_read_b64_tr_b16 v[86:87], v211 offset:0x1c00
	v_mfma_f32_32x32x16_bf16 v[48:63], v[92:95], v[116:119], v[48:63]
	ds_read_b64_tr_b16 v[88:89], v211 offset:0x2400
	ds_read_b64_tr_b16 v[90:91], v211 offset:0x2c00
	ds_read_b64_tr_b16 v[92:93], v211 offset:0x3400
	ds_read_b64_tr_b16 v[94:95], v211 offset:0x3c00
	s_waitcnt lgkmcnt(0)
	v_mfma_f32_32x32x16_bf16 v[32:47], v[80:83], v[124:127], v[32:47]
	v_exp_f32_e32 v80, v64
	v_exp_f32_e32 v81, v65
	v_exp_f32_e32 v64, v96
	v_exp_f32_e32 v65, v97
	v_exp_f32_e32 v82, v66
	v_exp_f32_e32 v83, v67
	v_exp_f32_e32 v66, v98
	v_exp_f32_e32 v67, v99
	v_mfma_f32_32x32x16_bf16 v[32:47], v[84:87], v[120:123], v[32:47]
	v_exp_f32_e32 v84, v68
	v_exp_f32_e32 v85, v69
	v_exp_f32_e32 v68, v100
	v_exp_f32_e32 v69, v101
	v_exp_f32_e32 v86, v70
	v_exp_f32_e32 v87, v71
	v_exp_f32_e32 v70, v102
	v_exp_f32_e32 v71, v103
	v_mfma_f32_32x32x16_bf16 v[32:47], v[88:91], v[112:115], v[32:47]
	v_exp_f32_e32 v194, v72
	v_exp_f32_e32 v195, v73
	ds_read_b64_tr_b16 v[72:73], v211 offset:0x600
	v_exp_f32_e32 v196, v74
	v_exp_f32_e32 v197, v75
	ds_read_b64_tr_b16 v[74:75], v211 offset:0xe00
	v_mfma_f32_32x32x16_bf16 v[32:47], v[92:95], v[116:119], v[32:47]
	v_exp_f32_e32 v92, v76
	v_exp_f32_e32 v93, v77
	ds_read_b64_tr_b16 v[76:77], v211 offset:0x1600
	v_exp_f32_e32 v94, v78
	v_exp_f32_e32 v95, v79
	ds_read_b64_tr_b16 v[78:79], v211 offset:0x1e00
	ds_read_b64_tr_b16 v[96:97], v211 offset:0x2600
	ds_read_b64_tr_b16 v[98:99], v211 offset:0x2e00
	ds_read_b64_tr_b16 v[100:101], v211 offset:0x3600
	ds_read_b64_tr_b16 v[102:103], v211 offset:0x3e00
	s_waitcnt lgkmcnt(0)
	v_mfma_f32_32x32x16_bf16 v[16:31], v[72:75], v[124:127], v[16:31]
	v_exp_f32_e32 v72, v104
	v_exp_f32_e32 v73, v105
	v_exp_f32_e32 v74, v106
	v_exp_f32_e32 v75, v107
	v_mfma_f32_32x32x16_bf16 v[16:31], v[76:79], v[120:123], v[16:31]
	v_exp_f32_e32 v76, v108
	v_exp_f32_e32 v77, v109
	v_exp_f32_e32 v78, v110
	v_exp_f32_e32 v79, v111
	s_barrier
	v_mfma_f32_32x32x16_bf16 v[16:31], v[96:99], v[112:115], v[16:31]
	s_waitcnt vmcnt(4)
	s_waitcnt vmcnt(7)
	ds_write_b128 v212, v[178:181] offset:16384
	s_waitcnt vmcnt(6)
	ds_write_b128 v213, v[182:185] offset:16384
	s_waitcnt vmcnt(5)
	ds_write_b128 v214, v[186:189] offset:49152
	s_waitcnt vmcnt(4)
	ds_write_b128 v215, v[190:193] offset:49152
	v_mfma_f32_32x32x16_bf16 v[16:31], v[100:103], v[116:119], v[16:31]
.LBB0_885:
	v_add_f32_e32 v96, v227, v228
	v_add_f32_e32 v96, v96, v217
	v_add_f32_e32 v217, v229, v233
	s_add_i32 s2, s39, 2
	s_add_i32 s3, s39, -1
	v_add_f32_e32 v217, v217, v96
	s_cmp_ge_u32 s3, s14
	s_waitcnt lgkmcnt(0)
	s_barrier
	s_cbranch_scc1 .LBB0_887
	s_mov_b32 s39, s2
	s_branch .LBB0_881
.LBB0_887:
	ds_read_b128 v[96:99], v216 offset:49152
	ds_read_b128 v[100:103], v216 offset:57344
	s_waitcnt lgkmcnt(1)
	v_mfma_f32_32x32x16_bf16 v[112:127], v[96:99], v[138:141], 0
	s_waitcnt lgkmcnt(0)
	v_mfma_f32_32x32x16_bf16 v[96:111], v[100:103], v[138:141], 0
	ds_read_b128 v[138:141], v218 offset:49152
	s_waitcnt vmcnt(3)
	ds_read_b128 v[162:165], v218 offset:57344
	v_add_f32_e32 v128, v64, v65
	v_add_f32_e32 v128, v66, v128
	s_waitcnt lgkmcnt(1)
	v_mfma_f32_32x32x16_bf16 v[112:127], v[138:141], v[154:157], v[112:127]
	v_add_f32_e32 v128, v67, v128
	v_add_f32_e32 v128, v68, v128
	v_add_f32_e32 v128, v69, v128
	v_add_f32_e32 v128, v70, v128
	v_add_f32_e32 v128, v71, v128
	s_waitcnt lgkmcnt(0)
	v_mfma_f32_32x32x16_bf16 v[96:111], v[162:165], v[154:157], v[96:111]
	ds_read_b128 v[138:141], v219 offset:49152
	ds_read_b128 v[154:157], v219 offset:57344
	s_waitcnt lgkmcnt(1)
	v_mfma_f32_32x32x16_bf16 v[112:127], v[138:141], v[158:161], v[112:127]
	s_waitcnt lgkmcnt(0)
	v_mfma_f32_32x32x16_bf16 v[96:111], v[154:157], v[158:161], v[96:111]
	ds_read_b128 v[138:141], v220 offset:49152
	ds_read_b128 v[154:157], v220 offset:57344
	s_waitcnt lgkmcnt(1)
	v_mfma_f32_32x32x16_bf16 v[112:127], v[138:141], v[150:153], v[112:127]
	s_waitcnt lgkmcnt(0)
	v_mfma_f32_32x32x16_bf16 v[96:111], v[154:157], v[150:153], v[96:111]
	ds_read_b128 v[138:141], v221 offset:49152
	ds_read_b128 v[150:153], v221 offset:57344
	s_waitcnt lgkmcnt(1)
	v_mfma_f32_32x32x16_bf16 v[112:127], v[138:141], v[146:149], v[112:127]
	s_waitcnt lgkmcnt(0)
	v_mfma_f32_32x32x16_bf16 v[96:111], v[150:153], v[146:149], v[96:111]
	ds_read_b128 v[138:141], v222 offset:49152
	ds_read_b128 v[146:149], v222 offset:57344
	s_waitcnt lgkmcnt(1)
	v_mfma_f32_32x32x16_bf16 v[112:127], v[138:141], v[142:145], v[112:127]
	s_waitcnt lgkmcnt(0)
	v_mfma_f32_32x32x16_bf16 v[96:111], v[146:149], v[142:145], v[96:111]
	ds_read_b128 v[138:141], v224 offset:49152
	ds_read_b128 v[142:145], v224 offset:57344
	s_waitcnt lgkmcnt(1)
	v_mfma_f32_32x32x16_bf16 v[112:127], v[138:141], v[134:137], v[112:127]
	s_waitcnt lgkmcnt(0)
	v_mfma_f32_32x32x16_bf16 v[96:111], v[142:145], v[134:137], v[96:111]
	ds_read_b128 v[134:137], v223 offset:49152
	ds_read_b128 v[138:141], v223 offset:57344
	s_waitcnt lgkmcnt(1)
	v_mfma_f32_32x32x16_bf16 v[112:127], v[134:137], v[130:133], v[112:127]
	s_waitcnt lgkmcnt(0)
	v_mfma_f32_32x32x16_bf16 v[96:111], v[138:141], v[130:133], v[96:111]
	v_add_f32_e32 v130, v72, v73
	v_add_f32_e32 v131, v80, v81
	v_add_f32_e32 v132, v194, v195
	v_add_f32_e32 v130, v74, v130
	v_add_f32_e32 v131, v82, v131
	v_add_f32_e32 v132, v196, v132
	v_add_f32_e32 v130, v75, v130
	v_add_f32_e32 v131, v83, v131
	v_add_f32_e32 v132, v197, v132
	v_add_f32_e32 v130, v76, v130
	v_add_f32_e32 v131, v84, v131
	v_add_f32_e32 v132, v92, v132
	v_add_f32_e32 v130, v77, v130
	v_add_f32_e32 v131, v85, v131
	v_add_f32_e32 v132, v93, v132
	v_add_f32_e32 v130, v78, v130
	v_add_f32_e32 v131, v86, v131
	v_add_f32_e32 v132, v94, v132
	v_add_f32_e32 v130, v79, v130
	v_add_f32_e32 v131, v87, v131
	v_add_f32_e32 v132, v95, v132
	v_add_f32_e32 v128, v130, v128
	v_add_f32_e32 v130, v132, v131
	v_add_f32_e32 v142, v128, v130
	v_mov_b32_e32 v143, v142
	v_cvt_pk_bf16_f32 v130, v64, v65
	v_cvt_pk_bf16_f32 v131, v66, v67
	v_cvt_pk_bf16_f32 v132, v68, v69
	v_cvt_pk_bf16_f32 v133, v70, v71
	v_cvt_pk_bf16_f32 v72, v72, v73
	v_cvt_pk_bf16_f32 v73, v74, v75
	v_cvt_pk_bf16_f32 v74, v76, v77
	v_cvt_pk_bf16_f32 v75, v78, v79
	s_nop 1
	v_permlane32_swap_b32_e32 v142, v143
	v_permlane32_swap_b32_e32 v72, v74
	v_permlane32_swap_b32_e32 v73, v75
	v_cvt_pk_bf16_f32 v138, v80, v81
	v_cvt_pk_bf16_f32 v139, v82, v83
	v_cvt_pk_bf16_f32 v140, v84, v85
	v_cvt_pk_bf16_f32 v141, v86, v87
	v_cvt_pk_bf16_f32 v134, v194, v195
	v_cvt_pk_bf16_f32 v135, v196, v197
	v_cvt_pk_bf16_f32 v136, v92, v93
	v_cvt_pk_bf16_f32 v137, v94, v95
	v_permlane32_swap_b32_e32 v130, v132
	v_permlane32_swap_b32_e32 v131, v133
	v_permlane32_swap_b32_e32 v138, v140
	v_permlane32_swap_b32_e32 v139, v141
	v_permlane32_swap_b32_e32 v134, v136
	v_permlane32_swap_b32_e32 v135, v137
	ds_read_b64_tr_b16 v[64:65], v209 offset:0
	ds_read_b64_tr_b16 v[66:67], v209 offset:0x800
	ds_read_b64_tr_b16 v[68:69], v209 offset:0x1000
	ds_read_b64_tr_b16 v[70:71], v209 offset:0x1800
	ds_read_b64_tr_b16 v[76:77], v209 offset:0x2000
	ds_read_b64_tr_b16 v[78:79], v209 offset:0x2800
	ds_read_b64_tr_b16 v[80:81], v209 offset:0x3000
	ds_read_b64_tr_b16 v[82:83], v209 offset:0x3800
	s_waitcnt lgkmcnt(0)
	s_nop 0
	v_mfma_f32_32x32x16_bf16 v[0:15], v[64:67], v[130:133], v[0:15]
	v_mfma_f32_32x32x16_bf16 v[0:15], v[68:71], v[72:75], v[0:15]
	v_mfma_f32_32x32x16_bf16 v[0:15], v[76:79], v[138:141], v[0:15]
	ds_read_b64_tr_b16 v[64:65], v209 offset:0x200
	ds_read_b64_tr_b16 v[66:67], v209 offset:0xa00
	ds_read_b64_tr_b16 v[68:69], v209 offset:0x1200
	v_mfma_f32_32x32x16_bf16 v[0:15], v[80:83], v[134:137], v[0:15]
	ds_read_b64_tr_b16 v[70:71], v209 offset:0x1a00
	ds_read_b64_tr_b16 v[76:77], v209 offset:0x2200
	ds_read_b64_tr_b16 v[78:79], v209 offset:0x2a00
	ds_read_b64_tr_b16 v[80:81], v209 offset:0x3200
	ds_read_b64_tr_b16 v[82:83], v209 offset:0x3a00
	s_waitcnt lgkmcnt(0)
	v_mfma_f32_32x32x16_bf16 v[48:63], v[64:67], v[130:133], v[48:63]
	v_mfma_f32_32x32x16_bf16 v[48:63], v[68:71], v[72:75], v[48:63]
	v_mfma_f32_32x32x16_bf16 v[48:63], v[76:79], v[138:141], v[48:63]
	v_mov_b32_e32 v128, 1.0
	v_mov_b32_e32 v208, 1.0
	ds_read_b64_tr_b16 v[64:65], v209 offset:0x400
	ds_read_b64_tr_b16 v[66:67], v209 offset:0xc00
	ds_read_b64_tr_b16 v[68:69], v209 offset:0x1400
	v_mfma_f32_32x32x16_bf16 v[48:63], v[80:83], v[134:137], v[48:63]
	ds_read_b64_tr_b16 v[70:71], v209 offset:0x1c00
	ds_read_b64_tr_b16 v[76:77], v209 offset:0x2400
	ds_read_b64_tr_b16 v[78:79], v209 offset:0x2c00
	ds_read_b64_tr_b16 v[80:81], v209 offset:0x3400
	ds_read_b64_tr_b16 v[82:83], v209 offset:0x3c00
	s_waitcnt lgkmcnt(0)
	v_mfma_f32_32x32x16_bf16 v[32:47], v[64:67], v[130:133], v[32:47]
	v_mov_b32_e32 v84, v100
	v_mov_b32_e32 v85, v101
	v_mov_b32_e32 v86, v102
	v_mov_b32_e32 v87, v103
	v_mov_b32_e32 v88, v104
	v_mov_b32_e32 v89, v105
	v_mov_b32_e32 v90, v106
	v_mov_b32_e32 v91, v107
	v_exp_f32_e32 v64, v112
	v_exp_f32_e32 v65, v113
	v_exp_f32_e32 v66, v114
	v_mfma_f32_32x32x16_bf16 v[32:47], v[68:71], v[72:75], v[32:47]
	v_exp_f32_e32 v67, v115
	v_exp_f32_e32 v68, v116
	v_exp_f32_e32 v69, v117
	v_exp_f32_e32 v70, v118
	v_exp_f32_e32 v71, v119
	v_mov_b32_e32 v94, v110
	v_mov_b32_e32 v95, v111
	v_mov_b32_e32 v92, v108
	v_mov_b32_e32 v93, v109
	v_mfma_f32_32x32x16_bf16 v[32:47], v[76:79], v[138:141], v[32:47]
	ds_read_b64_tr_b16 v[76:77], v209 offset:0x600
	ds_read_b64_tr_b16 v[78:79], v209 offset:0xe00
	v_mfma_f32_32x32x16_bf16 v[32:47], v[80:83], v[134:137], v[32:47]
	v_mov_b32_e32 v80, v96
	v_mov_b32_e32 v81, v97
	ds_read_b64_tr_b16 v[96:97], v209 offset:0x1600
	v_mov_b32_e32 v82, v98
	v_mov_b32_e32 v83, v99
	ds_read_b64_tr_b16 v[98:99], v209 offset:0x1e00
	ds_read_b64_tr_b16 v[100:101], v209 offset:0x2600
	ds_read_b64_tr_b16 v[102:103], v209 offset:0x2e00
	ds_read_b64_tr_b16 v[104:105], v209 offset:0x3600
	ds_read_b64_tr_b16 v[106:107], v209 offset:0x3e00
	s_waitcnt lgkmcnt(0)
	v_mfma_f32_32x32x16_bf16 v[16:31], v[76:79], v[130:133], v[16:31]
	v_exp_f32_e32 v76, v124
	v_exp_f32_e32 v77, v125
	v_exp_f32_e32 v78, v126
	v_exp_f32_e32 v79, v127
	v_mfma_f32_32x32x16_bf16 v[16:31], v[96:99], v[72:75], v[16:31]
	v_exp_f32_e32 v72, v120
	v_exp_f32_e32 v73, v121
	v_exp_f32_e32 v74, v122
	v_exp_f32_e32 v75, v123
	s_barrier
	v_mfma_f32_32x32x16_bf16 v[16:31], v[100:103], v[138:141], v[16:31]
	v_mfma_f32_32x32x16_bf16 v[16:31], v[104:107], v[134:137], v[16:31]
	s_branch .LBB0_873
	v_pk_mul_f32 v[14:15], v[14:15], v[128:129] op_sel_hi:[1,0]
	v_pk_mul_f32 v[12:13], v[12:13], v[128:129] op_sel_hi:[1,0]
	v_pk_mul_f32 v[10:11], v[10:11], v[128:129] op_sel_hi:[1,0]
	v_pk_mul_f32 v[8:9], v[8:9], v[128:129] op_sel_hi:[1,0]
	v_pk_mul_f32 v[6:7], v[6:7], v[128:129] op_sel_hi:[1,0]
	v_pk_mul_f32 v[4:5], v[4:5], v[128:129] op_sel_hi:[1,0]
	v_pk_mul_f32 v[2:3], v[2:3], v[128:129] op_sel_hi:[1,0]
	v_pk_mul_f32 v[0:1], v[0:1], v[128:129] op_sel_hi:[1,0]
	v_pk_mul_f32 v[62:63], v[62:63], v[128:129] op_sel_hi:[1,0]
	v_pk_mul_f32 v[60:61], v[60:61], v[128:129] op_sel_hi:[1,0]
	v_pk_mul_f32 v[58:59], v[58:59], v[128:129] op_sel_hi:[1,0]
	v_pk_mul_f32 v[56:57], v[56:57], v[128:129] op_sel_hi:[1,0]
	v_pk_mul_f32 v[54:55], v[54:55], v[128:129] op_sel_hi:[1,0]
	v_pk_mul_f32 v[52:53], v[52:53], v[128:129] op_sel_hi:[1,0]
	v_pk_mul_f32 v[50:51], v[50:51], v[128:129] op_sel_hi:[1,0]
	v_pk_mul_f32 v[48:49], v[48:49], v[128:129] op_sel_hi:[1,0]
	v_pk_mul_f32 v[46:47], v[128:129], v[46:47] op_sel_hi:[0,1]
	v_pk_mul_f32 v[44:45], v[128:129], v[44:45] op_sel_hi:[0,1]
	v_pk_mul_f32 v[42:43], v[128:129], v[42:43] op_sel_hi:[0,1]
	v_pk_mul_f32 v[40:41], v[128:129], v[40:41] op_sel_hi:[0,1]
	v_pk_mul_f32 v[38:39], v[128:129], v[38:39] op_sel_hi:[0,1]
	v_pk_mul_f32 v[36:37], v[128:129], v[36:37] op_sel_hi:[0,1]
	v_pk_mul_f32 v[34:35], v[128:129], v[34:35] op_sel_hi:[0,1]
	v_pk_mul_f32 v[32:33], v[128:129], v[32:33] op_sel_hi:[0,1]
	v_pk_mul_f32 v[30:31], v[128:129], v[30:31] op_sel_hi:[0,1]
	v_pk_mul_f32 v[28:29], v[128:129], v[28:29] op_sel_hi:[0,1]
	v_pk_mul_f32 v[26:27], v[128:129], v[26:27] op_sel_hi:[0,1]
	v_pk_mul_f32 v[24:25], v[128:129], v[24:25] op_sel_hi:[0,1]
	v_pk_mul_f32 v[22:23], v[128:129], v[22:23] op_sel_hi:[0,1]
	v_pk_mul_f32 v[20:21], v[128:129], v[20:21] op_sel_hi:[0,1]
	v_pk_mul_f32 v[18:19], v[128:129], v[18:19] op_sel_hi:[0,1]
	v_pk_mul_f32 v[16:17], v[128:129], v[16:17] op_sel_hi:[0,1]
	s_branch .LBB0_873
